# speedup vs baseline: 1.0636x; 1.0015x over previous
.LBB1_8:
	s_lshl_b32 s12, s62, 9
	v_lshl_add_u64 v[6:7], s[12:13], 4, v[210:211]
	v_add_co_u32_e32 v34, vcc, s52, v6
	s_mov_b32 s12, s13
	s_nop 0
	v_addc_co_u32_e32 v35, vcc, 0, v7, vcc
	global_load_dwordx4 v[2:5], v[34:35], off offset:-4096
	v_add_co_u32_e32 v36, vcc, s49, v6
	s_xor_b64 s[50:51], s[14:15], -1
	s_nop 0
	v_addc_co_u32_e32 v37, vcc, 0, v7, vcc
	global_load_dwordx4 v[6:9], v[36:37], off offset:1024
	global_load_dwordx4 v[10:13], v[36:37], off offset:2048
	global_load_dwordx4 v[14:17], v[34:35], off
	s_mov_b32 s14, s13
	s_mov_b32 s15, s13
	s_mov_b32 s16, s13
	s_mov_b32 s17, s13
	s_mov_b32 s18, s13
	s_mov_b32 s19, s13
	s_mov_b32 s20, s13
	s_mov_b32 s21, s13
	s_mov_b32 s22, s13
	s_mov_b32 s23, s13
	s_mov_b32 s24, s13
	s_mov_b32 s25, s13
	s_mov_b32 s26, s13
	s_mov_b32 s27, s13
	s_waitcnt vmcnt(3) lgkmcnt(7)
	v_mfma_f32_32x32x16_f16 v[18:33], v[2:5], v[146:149], 0
	global_load_dwordx4 v[2:5], v[36:37], off offset:3072
	s_waitcnt vmcnt(3) lgkmcnt(6)
	v_mfma_f32_32x32x16_f16 v[18:33], v[6:9], v[150:153], v[18:33]
	global_load_dwordx4 v[6:9], v[34:35], off offset:1024
	s_waitcnt vmcnt(3) lgkmcnt(5)
	v_mfma_f32_32x32x16_f16 v[18:33], v[10:13], v[154:157], v[18:33]
	global_load_dwordx4 v[10:13], v[34:35], off offset:2048
	s_nop 0
	global_load_dwordx4 v[34:37], v[34:35], off offset:3072
	s_waitcnt vmcnt(3) lgkmcnt(4)
	v_mfma_f32_32x32x16_f16 v[18:33], v[2:5], v[158:161], v[18:33]
	s_waitcnt lgkmcnt(3)
	v_mfma_f32_32x32x16_f16 v[18:33], v[14:17], v[162:165], v[18:33]
	s_waitcnt vmcnt(2) lgkmcnt(2)
	v_mfma_f32_32x32x16_f16 v[18:33], v[6:9], v[166:169], v[18:33]
	s_waitcnt vmcnt(1) lgkmcnt(1)
	v_mfma_f32_32x32x16_f16 v[18:33], v[10:13], v[170:173], v[18:33]
	v_mov_b64_e32 v[2:3], s[12:13]
	v_mov_b64_e32 v[4:5], s[14:15]
	v_mov_b64_e32 v[6:7], s[16:17]
	v_mov_b64_e32 v[8:9], s[18:19]
	v_mov_b64_e32 v[10:11], s[20:21]
	v_mov_b64_e32 v[12:13], s[22:23]
	v_mov_b64_e32 v[14:15], s[24:25]
	s_waitcnt vmcnt(0) lgkmcnt(0)
	v_mfma_f32_32x32x16_f16 v[18:33], v[34:37], v[174:177], v[18:33]
	v_mov_b64_e32 v[16:17], s[26:27]
	s_mul_i32 s12, s62, 20
	s_lshl_b64 s[14:15], s[12:13], 2
	s_add_u32 s14, s10, s14
	s_addc_u32 s15, s11, s15
	s_load_dwordx16 s[16:31], s[14:15], 0x0
	s_load_dwordx4 s[40:43], s[14:15], 0x40
	s_mul_i32 s12, s62, 0x1b0000
	s_nop 3
	ds_bpermute_b32 v34, v225, v18
	ds_bpermute_b32 v35, v225, v19
	ds_bpermute_b32 v36, v225, v20
	ds_bpermute_b32 v37, v225, v21
	ds_bpermute_b32 v38, v225, v22
	ds_bpermute_b32 v39, v225, v23
	ds_bpermute_b32 v40, v225, v24
	ds_bpermute_b32 v41, v225, v25
	ds_bpermute_b32 v42, v225, v26
	ds_bpermute_b32 v43, v225, v27
	ds_bpermute_b32 v44, v225, v28
	ds_bpermute_b32 v45, v225, v29
	ds_bpermute_b32 v46, v225, v30
	ds_bpermute_b32 v47, v225, v31
	ds_bpermute_b32 v48, v225, v32
	ds_bpermute_b32 v49, v225, v33
	s_waitcnt lgkmcnt(0)
	v_cndmask_b32_e64 v50, v34, v18, s[0:1]
	v_cndmask_b32_e64 v19, v35, v19, s[0:1]
	v_cndmask_b32_e64 v20, v36, v20, s[0:1]
	v_cndmask_b32_e64 v21, v37, v21, s[0:1]
	v_cndmask_b32_e64 v18, v18, v34, s[0:1]
	v_cndmask_b32_e64 v34, v38, v22, s[0:1]
	v_cndmask_b32_e64 v23, v39, v23, s[0:1]
	v_cndmask_b32_e64 v24, v40, v24, s[0:1]
	v_cndmask_b32_e64 v25, v41, v25, s[0:1]
	v_cndmask_b32_e64 v22, v22, v38, s[0:1]
	v_add_f32_e32 v37, s16, v50
	v_add_f32_e32 v19, s17, v19
	v_add_f32_e32 v20, s18, v20
	v_add_f32_e32 v21, s19, v21
	v_add_f32_e32 v34, s21, v34
	v_add_f32_e32 v23, s22, v23
	v_add_f32_e32 v24, s23, v24
	v_add_f32_e32 v25, s24, v25
	v_cndmask_b32_e64 v35, v42, v26, s[0:1]
	v_cndmask_b32_e64 v27, v43, v27, s[0:1]
	v_cndmask_b32_e64 v28, v44, v28, s[0:1]
	v_cndmask_b32_e64 v29, v45, v29, s[0:1]
	v_add_f32_e32 v18, s20, v18
	v_add_f32_e32 v22, s25, v22
	v_max_f32_e32 v38, v37, v19
	v_max_f32_e32 v39, v20, v21
	v_max_f32_e32 v40, v34, v23
	v_max_f32_e32 v41, v24, v25
	v_cndmask_b32_e64 v26, v26, v42, s[0:1]
	v_cndmask_b32_e64 v36, v46, v30, s[0:1]
	v_cndmask_b32_e64 v31, v47, v31, s[0:1]
	v_cndmask_b32_e64 v32, v48, v32, s[0:1]
	v_add_f32_e32 v35, s26, v35
	v_add_f32_e32 v27, s27, v27
	v_add_f32_e32 v28, s28, v28
	v_add_f32_e32 v29, s29, v29
	v_max3_f32 v38, v38, v39, v18
	v_max3_f32 v39, v40, v41, v22
	v_cndmask_b32_e64 v33, v49, v33, s[0:1]
	v_add_f32_e32 v26, s30, v26
	v_add_f32_e32 v36, s31, v36
	v_add_f32_e32 v31, s40, v31
	v_add_f32_e32 v32, s41, v32
	v_max_f32_e32 v42, v35, v27
	v_max_f32_e32 v43, v28, v29
	v_sub_f32_e32 v34, v34, v39
	v_add_f32_e32 v33, s42, v33
	v_cndmask_b32_e64 v30, v30, v46, s[0:1]
	v_max3_f32 v40, v42, v43, v26
	v_sub_f32_e32 v37, v37, v38
	v_sub_f32_e32 v23, v23, v39
	v_mul_f32_e32 v34, 0x3fb8aa3b, v34
	v_add_f32_e32 v30, s43, v30
	v_max_f32_e32 v41, v36, v31
	v_max_f32_e32 v42, v32, v33
	v_sub_f32_e32 v19, v19, v38
	v_sub_f32_e32 v24, v24, v39
	v_sub_f32_e32 v35, v35, v40
	v_mul_f32_e32 v37, 0x3fb8aa3b, v37
	v_mul_f32_e32 v23, 0x3fb8aa3b, v23
	v_exp_f32_e32 v34, v34
	v_max3_f32 v41, v41, v42, v30
	v_sub_f32_e32 v20, v20, v38
	v_sub_f32_e32 v25, v25, v39
	v_sub_f32_e32 v27, v27, v40
	v_mul_f32_e32 v19, 0x3fb8aa3b, v19
	v_mul_f32_e32 v24, 0x3fb8aa3b, v24
	v_mul_f32_e32 v35, 0x3fb8aa3b, v35
	v_exp_f32_e32 v37, v37
	v_exp_f32_e32 v23, v23
	v_sub_f32_e32 v36, v36, v41
	v_sub_f32_e32 v21, v21, v38
	v_sub_f32_e32 v22, v22, v39
	v_sub_f32_e32 v28, v28, v40
	v_mul_f32_e32 v20, 0x3fb8aa3b, v20
	v_mul_f32_e32 v25, 0x3fb8aa3b, v25
	v_mul_f32_e32 v27, 0x3fb8aa3b, v27
	v_exp_f32_e32 v19, v19
	v_exp_f32_e32 v24, v24
	v_exp_f32_e32 v35, v35
	v_mul_f32_e32 v36, 0x3fb8aa3b, v36
	v_sub_f32_e32 v31, v31, v41
	v_sub_f32_e32 v18, v18, v38
	v_sub_f32_e32 v29, v29, v40
	v_mul_f32_e32 v21, 0x3fb8aa3b, v21
	v_mul_f32_e32 v22, 0x3fb8aa3b, v22
	v_mul_f32_e32 v28, 0x3fb8aa3b, v28
	v_exp_f32_e32 v20, v20
	v_exp_f32_e32 v25, v25
	v_exp_f32_e32 v27, v27
	v_exp_f32_e32 v36, v36
	v_mul_f32_e32 v31, 0x3fb8aa3b, v31
	v_sub_f32_e32 v32, v32, v41
	v_sub_f32_e32 v26, v26, v40
	v_mul_f32_e32 v18, 0x3fb8aa3b, v18
	v_mul_f32_e32 v29, 0x3fb8aa3b, v29
	v_exp_f32_e32 v21, v21
	v_exp_f32_e32 v22, v22
	v_exp_f32_e32 v28, v28
	v_add_f32_e32 v39, 0, v34
	v_exp_f32_e32 v31, v31
	v_mul_f32_e32 v32, 0x3fb8aa3b, v32
	v_sub_f32_e32 v33, v33, v41
	v_mul_f32_e32 v26, 0x3fb8aa3b, v26
	v_exp_f32_e32 v18, v18
	v_exp_f32_e32 v29, v29
	v_add_f32_e32 v38, 0, v37
	v_add_f32_e32 v39, v23, v39
	v_exp_f32_e32 v32, v32
	v_mul_f32_e32 v33, 0x3fb8aa3b, v33
	v_sub_f32_e32 v30, v30, v41
	v_exp_f32_e32 v26, v26
	v_add_f32_e32 v40, 0, v35
	v_add_f32_e32 v38, v19, v38
	v_add_f32_e32 v39, v24, v39
	v_exp_f32_e32 v33, v33
	v_mul_f32_e32 v30, 0x3fb8aa3b, v30
	v_add_f32_e32 v40, v27, v40
	v_add_f32_e32 v38, v20, v38
	v_add_f32_e32 v39, v25, v39
	v_add_f32_e32 v42, 0, v36
	v_exp_f32_e32 v30, v30
	v_add_f32_e32 v38, v21, v38
	v_add_f32_e32 v39, v22, v39
	v_add_f32_e32 v40, v28, v40
	v_add_f32_e32 v41, v31, v42
	v_add_f32_e32 v38, v18, v38
	v_rcp_f32_e32 v39, v39
	v_add_f32_e32 v40, v29, v40
	v_add_f32_e32 v41, v32, v41
	v_rcp_f32_e32 v38, v38
	v_add_f32_e32 v40, v26, v40
	v_add_f32_e32 v41, v33, v41
	v_rcp_f32_e32 v40, v40
	v_add_f32_e32 v41, v30, v41
	v_rcp_f32_e32 v41, v41
	v_mul_f32_e32 v34, v34, v39
	v_mul_f32_e32 v23, v23, v39
	v_fmac_f32_e32 v34, v37, v38
	v_fmac_f32_e32 v23, v19, v38
	v_mul_f32_e32 v24, v24, v39
	v_fmac_f32_e32 v34, v35, v40
	v_fmac_f32_e32 v23, v27, v40
	v_mul_f32_e32 v22, v22, v39
	v_mul_f32_e32 v29, v29, v40
	v_fmac_f32_e32 v34, v36, v41
	v_fmac_f32_e32 v23, v31, v41
	v_fmac_f32_e32 v24, v20, v38
	v_fmac_f32_e32 v24, v28, v40
	v_cndmask_b32_e64 v20, v22, v34, s[4:5]
	v_cndmask_b32_e64 v22, v29, v23, s[4:5]
	v_mul_f32_e32 v21, v21, v38
	v_mul_f32_e32 v18, v18, v38
	v_mul_f32_e32 v25, v25, v39
	v_mul_f32_e32 v26, v26, v40
	v_mul_f32_e32 v33, v33, v41
	v_mul_f32_e32 v30, v30, v41
	v_fmac_f32_e32 v24, v32, v41
	v_mul_f32_e32 v20, 0x3e800000, v20
	v_mul_f32_e32 v22, 0x3e800000, v22
	v_mul_f32_e32 v19, 0x3e800000, v25
	ds_write2st64_b32 v222, v20, v22 offset1:8
	v_cndmask_b32_e64 v20, v26, v24, s[4:5]
	v_cndmask_b32_e64 v21, v33, v21, s[4:5]
	v_cndmask_b32_e64 v18, v30, v18, s[4:5]
	v_mul_f32_e32 v20, 0x3e800000, v20
	v_mul_f32_e32 v21, 0x3e800000, v21
	v_mul_f32_e32 v18, 0x3e800000, v18
	v_cndmask_b32_e64 v19, 0, v19, s[4:5]
	ds_write2st64_b32 v222, v20, v21 offset0:16 offset1:24
	ds_write2st64_b32 v222, v18, v19 offset0:32 offset1:40
	s_mul_hi_u32 s14, s62, 0x1b0000
	s_add_u32 s12, s44, s12
	v_mov_b64_e32 v[64:65], v[16:17]
	v_mov_b64_e32 v[48:49], v[16:17]
	v_mov_b64_e32 v[32:33], v[16:17]
	s_addc_u32 s16, s45, s14
	s_mov_b32 s17, 0
	v_mov_b64_e32 v[62:63], v[14:15]
	v_mov_b64_e32 v[60:61], v[12:13]
	v_mov_b64_e32 v[58:59], v[10:11]
	v_mov_b64_e32 v[56:57], v[8:9]
	v_mov_b64_e32 v[54:55], v[6:7]
	v_mov_b64_e32 v[52:53], v[4:5]
	v_mov_b64_e32 v[50:51], v[2:3]
	v_mov_b64_e32 v[46:47], v[14:15]
	v_mov_b64_e32 v[44:45], v[12:13]
	v_mov_b64_e32 v[42:43], v[10:11]
	v_mov_b64_e32 v[40:41], v[8:9]
	v_mov_b64_e32 v[38:39], v[6:7]
	v_mov_b64_e32 v[36:37], v[4:5]
	v_mov_b64_e32 v[34:35], v[2:3]
	v_mov_b64_e32 v[30:31], v[14:15]
	v_mov_b64_e32 v[28:29], v[12:13]
	v_mov_b64_e32 v[26:27], v[10:11]
	v_mov_b64_e32 v[24:25], v[8:9]
	v_mov_b64_e32 v[22:23], v[6:7]
	v_mov_b64_e32 v[20:21], v[4:5]
	v_mov_b64_e32 v[18:19], v[2:3]
	s_mov_b32 s18, 0
	s_mul_i32 s25, s33, 0x9000
	s_add_i32 s26, s33, -1
	s_cmp_eq_u32 s33, 0
	s_cselect_b32 s26, 2, s26
	s_mul_i32 s26, s26, 0x9000
	s_cmp_lg_u32 s4, 0
	s_cselect_b32 s27, 0x7fffffff, 40
	v_readfirstlane_b32 s28, v0
	s_lshl_b32 s28, s28, 4
	s_and_b32 s29, s28, 0xfffff000
	s_and_b32 s28, s28, 0xfffffc00
	s_add_i32 s28, s28, 0x8000
	s_sub_i32 s29, 0x8000, s29
	s_add_i32 s22, s25, 0x8000
	v_add_u32_e32 v189, s22, v246
	v_add_u32_e32 v248, s25, v247
	ds_read_b128 v[130:133], v189 offset:32768
	ds_read_b128 v[134:137], v189 offset:32800
	ds_read_b128 v[138:141], v189 offset:32832
	ds_read_b128 v[142:145], v189 offset:32864
	ds_read_b128 v[190:193], v248 offset:32768
	ds_read_b128 v[194:197], v248 offset:33792
	ds_read_b128 v[198:201], v248 offset:34816
	ds_read_b128 v[202:205], v248 offset:35840
	ds_read_b128 v[212:215], v248 offset:36864
	ds_read_b128 v[228:231], v248 offset:37888
	ds_read_b128 v[232:235], v248 offset:38912
	ds_read_b128 v[236:239], v248 offset:39936
	s_branch .LBB1_10
	.p2align	6
